# speedup vs baseline: 1.0041x; 1.0003x over previous
_Z11attn_kernelPKtS0_PKfS2_S2_PfS3_:
	s_load_dwordx4 s[12:15], s[0:1], 0x8
	v_lshlrev_b32_e32 v1, 4, v0
	v_or_b32_e32 v10, 0x4000, v1
	v_or_b32_e32 v18, 0x8000, v1
	v_or_b32_e32 v19, 0xc000, v1
	v_or_b32_e32 v30, 0x10000, v1
	v_or_b32_e32 v38, 0x1c000, v1
	s_movk_i32 s3, 0x380
	v_cmp_gt_u32_e32 vcc, s3, v0
	v_readfirstlane_b32 s16, v0
	v_or_b32_e32 v31, 0x14000, v1
	v_or_b32_e32 v33, 0x18000, v1
	s_lshl_b32 s16, s16, 4
	s_waitcnt lgkmcnt(0)
	s_mov_b32 m0, s16
	s_nop 0
	global_load_lds_dwordx4 v1, s[12:13]
	s_add_u32 m0, s16, 0x4000
	s_nop 0
	global_load_lds_dwordx4 v10, s[12:13]
	s_add_u32 m0, s16, 0x8000
	s_nop 0
	global_load_lds_dwordx4 v18, s[12:13]
	s_add_u32 m0, s16, 0xc000
	s_nop 0
	global_load_lds_dwordx4 v19, s[12:13]
	s_add_u32 m0, s16, 0x10000
	s_nop 0
	global_load_lds_dwordx4 v30, s[12:13]
	s_add_u32 m0, s16, 0x14000
	s_nop 0
	global_load_lds_dwordx4 v31, s[12:13]
	s_add_u32 m0, s16, 0x18000
	s_nop 0
	global_load_lds_dwordx4 v33, s[12:13]
	s_and_saveexec_b64 s[4:5], vcc
	s_cbranch_execz .Lattn_s8
	s_add_u32 m0, s16, 0x1c000
	s_nop 0
	global_load_lds_dwordx4 v38, s[12:13]
.Lattn_s8:
	s_or_b64 exec, exec, s[4:5]
	s_load_dwordx2 s[12:13], s[0:1], 0x0
	s_load_dwordx8 s[4:11], s[0:1], 0x18
	v_and_b32_e32 v108, 15, v0
	v_bfe_u32 v1, v0, 4, 5
	v_mul_u32_u24_e32 v3, 0x2d0, v1
	v_lshlrev_b32_e32 v4, 1, v108
	v_add3_u32 v3, v3, v4, 0
	v_or_b32_e32 v2, -16, v108
	v_add_u32_e32 v4, 0x17600, v3
	v_mov_b32_e32 v3, 0
	s_mov_b64 s[0:1], 0
	s_movk_i32 s3, 0x14f
	s_waitcnt vmcnt(0) lgkmcnt(0)
	s_barrier
	ds_read_u16 v72, v4
	ds_read_u16 v73, v4 offset:32
	ds_read_u16 v74, v4 offset:64
	ds_read_u16 v75, v4 offset:96
	ds_read_u16 v76, v4 offset:128
	ds_read_u16 v77, v4 offset:160
	ds_read_u16 v78, v4 offset:192
	ds_read_u16 v79, v4 offset:224
	ds_read_u16 v80, v4 offset:256
	ds_read_u16 v81, v4 offset:288
	ds_read_u16 v82, v4 offset:320
	ds_read_u16 v83, v4 offset:352
	ds_read_u16 v84, v4 offset:384
	ds_read_u16 v85, v4 offset:416
	ds_read_u16 v86, v4 offset:448
	ds_read_u16 v87, v4 offset:480
	ds_read_u16 v88, v4 offset:512
	ds_read_u16 v89, v4 offset:544
	ds_read_u16 v90, v4 offset:576
	ds_read_u16 v91, v4 offset:608
	ds_read_u16 v92, v4 offset:640
	ds_read_u16 v93, v4 offset:672
	s_waitcnt lgkmcnt(11)
	v_lshlrev_b32_e32 v72, 16, v72
	v_max_f32_e32 v72, v72, v72
	v_max_f32_e32 v72, 0, v72
	v_add_f32_e32 v3, v3, v72
	v_lshlrev_b32_e32 v73, 16, v73
	v_max_f32_e32 v73, v73, v73
	v_max_f32_e32 v73, 0, v73
	v_add_f32_e32 v3, v3, v73
	v_lshlrev_b32_e32 v74, 16, v74
	v_max_f32_e32 v74, v74, v74
	v_max_f32_e32 v74, 0, v74
	v_add_f32_e32 v3, v3, v74
	v_lshlrev_b32_e32 v75, 16, v75
	v_max_f32_e32 v75, v75, v75
	v_max_f32_e32 v75, 0, v75
	v_add_f32_e32 v3, v3, v75
	v_lshlrev_b32_e32 v76, 16, v76
	v_max_f32_e32 v76, v76, v76
	v_max_f32_e32 v76, 0, v76
	v_add_f32_e32 v3, v3, v76
	v_lshlrev_b32_e32 v77, 16, v77
	v_max_f32_e32 v77, v77, v77
	v_max_f32_e32 v77, 0, v77
	v_add_f32_e32 v3, v3, v77
	v_lshlrev_b32_e32 v78, 16, v78
	v_max_f32_e32 v78, v78, v78
	v_max_f32_e32 v78, 0, v78
	v_add_f32_e32 v3, v3, v78
	v_lshlrev_b32_e32 v79, 16, v79
	v_max_f32_e32 v79, v79, v79
	v_max_f32_e32 v79, 0, v79
	v_add_f32_e32 v3, v3, v79
	v_lshlrev_b32_e32 v80, 16, v80
	v_max_f32_e32 v80, v80, v80
	v_max_f32_e32 v80, 0, v80
	v_add_f32_e32 v3, v3, v80
	v_lshlrev_b32_e32 v81, 16, v81
	v_max_f32_e32 v81, v81, v81
	v_max_f32_e32 v81, 0, v81
	v_add_f32_e32 v3, v3, v81
	v_lshlrev_b32_e32 v82, 16, v82
	v_max_f32_e32 v82, v82, v82
	v_max_f32_e32 v82, 0, v82
	v_add_f32_e32 v3, v3, v82
	s_waitcnt lgkmcnt(0)
	v_lshlrev_b32_e32 v83, 16, v83
	v_max_f32_e32 v83, v83, v83
	v_max_f32_e32 v83, 0, v83
	v_add_f32_e32 v3, v3, v83
	v_lshlrev_b32_e32 v84, 16, v84
	v_max_f32_e32 v84, v84, v84
	v_max_f32_e32 v84, 0, v84
	v_add_f32_e32 v3, v3, v84
	v_lshlrev_b32_e32 v85, 16, v85
	v_max_f32_e32 v85, v85, v85
	v_max_f32_e32 v85, 0, v85
	v_add_f32_e32 v3, v3, v85
	v_lshlrev_b32_e32 v86, 16, v86
	v_max_f32_e32 v86, v86, v86
	v_max_f32_e32 v86, 0, v86
	v_add_f32_e32 v3, v3, v86
	v_lshlrev_b32_e32 v87, 16, v87
	v_max_f32_e32 v87, v87, v87
	v_max_f32_e32 v87, 0, v87
	v_add_f32_e32 v3, v3, v87
	v_lshlrev_b32_e32 v88, 16, v88
	v_max_f32_e32 v88, v88, v88
	v_max_f32_e32 v88, 0, v88
	v_add_f32_e32 v3, v3, v88
	v_lshlrev_b32_e32 v89, 16, v89
	v_max_f32_e32 v89, v89, v89
	v_max_f32_e32 v89, 0, v89
	v_add_f32_e32 v3, v3, v89
	v_lshlrev_b32_e32 v90, 16, v90
	v_max_f32_e32 v90, v90, v90
	v_max_f32_e32 v90, 0, v90
	v_add_f32_e32 v3, v3, v90
	v_lshlrev_b32_e32 v91, 16, v91
	v_max_f32_e32 v91, v91, v91
	v_max_f32_e32 v91, 0, v91
	v_add_f32_e32 v3, v3, v91
	v_lshlrev_b32_e32 v92, 16, v92
	v_max_f32_e32 v92, v92, v92
	v_max_f32_e32 v92, 0, v92
	v_add_f32_e32 v3, v3, v92
	v_lshlrev_b32_e32 v93, 16, v93
	v_max_f32_e32 v93, v93, v93
	v_max_f32_e32 v93, 0, v93
	v_add_f32_e32 v3, v3, v93
	s_or_b64 exec, exec, s[0:1]
	v_add_f32_dpp v2, v3, v3 quad_perm:[1,0,3,2] row_mask:0xf bank_mask:0xf bound_ctrl:1
	v_cmp_eq_u32_e32 vcc, 0, v108
	s_nop 0
	v_add_f32_dpp v2, v2, v2 quad_perm:[2,3,0,1] row_mask:0xf bank_mask:0xf bound_ctrl:1
	s_nop 1
	v_add_f32_dpp v2, v2, v2 row_half_mirror row_mask:0xf bank_mask:0xf bound_ctrl:1
	s_nop 1
	v_mov_b32_dpp v3, v2 row_mirror row_mask:0xf bank_mask:0xf bound_ctrl:1
	s_and_saveexec_b64 s[0:1], vcc
	s_cbranch_execz .LBB2_6
	v_add_f32_e32 v2, v2, v3
	v_mov_b32_e32 v3, 0x3c23d70a
	v_lshl_add_u32 v1, v1, 2, 0
	v_fmac_f32_e32 v3, 0x3f804189, v2
	v_add_u32_e32 v1, 0x1f780, v1
	v_xor_b32_e32 v2, 0x80000000, v3
	ds_write_b32 v1, v2
